# expert-weight conversion f32 loads marked nt (read-once stream), on top of the P6/P7 epilogue and attention K-hoist edits
# speedup vs baseline: 1.0157x; 1.0027x over previous
.LBB0_496:
	v_or_b32_e32 v1, s15, v69
	v_lshlrev_b32_e32 v2, 2, v1
	v_mov_b32_e32 v3, v0
	v_lshl_add_u64 v[36:37], s[12:13], 0, v[2:3]
	v_mov_b32_e32 v2, v0
	v_cmp_gt_u32_e32 vcc, s14, v1
	v_mov_b32_e32 v1, v0
	v_mov_b64_e32 v[6:7], v[2:3]
	v_mov_b64_e32 v[10:11], v[2:3]
	v_add_u32_e32 v38, s6, v68
	v_mov_b64_e32 v[4:5], v[0:1]
	v_mov_b64_e32 v[8:9], v[0:1]
	s_and_saveexec_b64 s[12:13], vcc
	s_cbranch_execz .LBB0_498
	v_mad_i64_i32 v[4:5], s[18:19], s14, v38, 0
	v_lshl_add_u64 v[12:13], v[4:5], 2, v[36:37]
	v_add_u32_e32 v4, 8, v38
	v_mad_i64_i32 v[4:5], s[18:19], s14, v4, 0
	v_lshl_add_u64 v[14:15], v[4:5], 2, v[36:37]
	global_load_dwordx4 v[4:7], v[12:13], off nt
	global_load_dwordx4 v[8:11], v[14:15], off nt
.LBB0_498:
	s_or_b64 exec, exec, s[12:13]
	v_mov_b64_e32 v[14:15], v[2:3]
	v_mov_b64_e32 v[18:19], v[2:3]
	v_mov_b64_e32 v[12:13], v[0:1]
	v_mov_b64_e32 v[16:17], v[0:1]
	s_and_saveexec_b64 s[12:13], vcc
	s_cbranch_execz .LBB0_500
	v_add_u32_e32 v1, 16, v38
	v_mad_i64_i32 v[2:3], s[18:19], s14, v1, 0
	v_add_u32_e32 v1, 24, v38
	v_lshl_add_u64 v[2:3], v[2:3], 2, v[36:37]
	v_mad_i64_i32 v[12:13], s[18:19], s14, v1, 0
	v_lshl_add_u64 v[20:21], v[12:13], 2, v[36:37]
	global_load_dwordx4 v[12:15], v[2:3], off nt
	global_load_dwordx4 v[16:19], v[20:21], off nt
.LBB0_500:
	s_or_b64 exec, exec, s[12:13]
	v_mov_b32_e32 v2, v0
	v_mov_b32_e32 v3, v0
	v_mov_b32_e32 v1, v0
	v_mov_b64_e32 v[22:23], v[2:3]
	v_mov_b64_e32 v[26:27], v[2:3]
	v_mov_b64_e32 v[20:21], v[0:1]
	v_mov_b64_e32 v[24:25], v[0:1]
	s_and_saveexec_b64 s[12:13], vcc
	s_cbranch_execz .LBB0_502
	v_add_u32_e32 v20, 32, v38
	v_mad_i64_i32 v[20:21], s[18:19], s14, v20, 0
	v_lshl_add_u64 v[28:29], v[20:21], 2, v[36:37]
	v_add_u32_e32 v20, 40, v38
	v_mad_i64_i32 v[20:21], s[18:19], s14, v20, 0
	v_lshl_add_u64 v[30:31], v[20:21], 2, v[36:37]
	global_load_dwordx4 v[20:23], v[28:29], off nt
	global_load_dwordx4 v[24:27], v[30:31], off nt
.LBB0_502:
	s_or_b64 exec, exec, s[12:13]
	v_mov_b64_e32 v[30:31], v[2:3]
	v_mov_b64_e32 v[34:35], v[2:3]
	v_mov_b64_e32 v[28:29], v[0:1]
	v_mov_b64_e32 v[32:33], v[0:1]
	s_and_saveexec_b64 s[12:13], vcc
	s_cbranch_execz .LBB0_504
	v_add_u32_e32 v1, 48, v38
	v_mad_i64_i32 v[2:3], s[18:19], s14, v1, 0
	v_add_u32_e32 v1, 56, v38
	v_lshl_add_u64 v[2:3], v[2:3], 2, v[36:37]
	v_mad_i64_i32 v[28:29], s[14:15], s14, v1, 0
	v_lshl_add_u64 v[36:37], v[28:29], 2, v[36:37]
	global_load_dwordx4 v[28:31], v[2:3], off nt
	global_load_dwordx4 v[32:35], v[36:37], off nt

.LBB0_512:
	v_or_b32_e32 v2, s38, v69
	v_mov_b32_e32 v3, v0
	v_cmp_gt_u32_e32 vcc, s19, v2
	v_lshl_add_u64 v[78:79], v[2:3], 2, s[16:17]
	v_mov_b32_e32 v2, v0
	v_mov_b32_e32 v1, v0
	v_mov_b64_e32 v[38:39], v[2:3]
	v_mov_b64_e32 v[42:43], v[2:3]
	v_add_u32_e32 v77, s6, v68
	v_mov_b64_e32 v[36:37], v[0:1]
	v_mov_b64_e32 v[40:41], v[0:1]
	s_and_saveexec_b64 s[16:17], vcc
	s_cbranch_execz .LBB0_514
	v_mad_i64_i32 v[36:37], s[38:39], s19, v77, 0
	v_lshl_add_u64 v[44:45], v[36:37], 2, v[78:79]
	v_add_u32_e32 v36, 8, v77
	v_mad_i64_i32 v[36:37], s[38:39], s19, v36, 0
	v_lshl_add_u64 v[46:47], v[36:37], 2, v[78:79]
	global_load_dwordx4 v[36:39], v[44:45], off nt
	global_load_dwordx4 v[40:43], v[46:47], off nt
.LBB0_514:
	s_or_b64 exec, exec, s[16:17]
	v_mov_b64_e32 v[46:47], v[2:3]
	v_mov_b64_e32 v[50:51], v[2:3]
	v_mov_b64_e32 v[44:45], v[0:1]
	v_mov_b64_e32 v[48:49], v[0:1]
	s_and_saveexec_b64 s[16:17], vcc
	s_cbranch_execz .LBB0_516
	v_add_u32_e32 v1, 16, v77
	v_mad_i64_i32 v[2:3], s[38:39], s19, v1, 0
	v_add_u32_e32 v1, 24, v77
	v_lshl_add_u64 v[2:3], v[2:3], 2, v[78:79]
	v_mad_i64_i32 v[44:45], s[38:39], s19, v1, 0
	v_lshl_add_u64 v[52:53], v[44:45], 2, v[78:79]
	global_load_dwordx4 v[44:47], v[2:3], off nt
	global_load_dwordx4 v[48:51], v[52:53], off nt
.LBB0_516:
	s_or_b64 exec, exec, s[16:17]
	v_mov_b32_e32 v2, v0
	v_mov_b32_e32 v3, v0
	v_mov_b32_e32 v1, v0
	v_mov_b64_e32 v[54:55], v[2:3]
	v_mov_b64_e32 v[58:59], v[2:3]
	v_mov_b64_e32 v[52:53], v[0:1]
	v_mov_b64_e32 v[56:57], v[0:1]
	s_and_saveexec_b64 s[16:17], vcc
	s_cbranch_execz .LBB0_518
	v_add_u32_e32 v52, 32, v77
	v_mad_i64_i32 v[52:53], s[38:39], s19, v52, 0
	v_lshl_add_u64 v[60:61], v[52:53], 2, v[78:79]
	v_add_u32_e32 v52, 40, v77
	v_mad_i64_i32 v[52:53], s[38:39], s19, v52, 0
	v_lshl_add_u64 v[62:63], v[52:53], 2, v[78:79]
	global_load_dwordx4 v[52:55], v[60:61], off nt
	global_load_dwordx4 v[56:59], v[62:63], off nt
.LBB0_518:
	s_or_b64 exec, exec, s[16:17]
	s_lshl_b64 s[16:17], s[6:7], 1
	s_add_u32 s14, s14, s16
	v_mov_b64_e32 v[62:63], v[2:3]
	v_mov_b64_e32 v[66:67], v[2:3]
	s_addc_u32 s15, s15, s17
	v_mov_b64_e32 v[60:61], v[0:1]
	v_mov_b64_e32 v[64:65], v[0:1]
	s_and_saveexec_b64 s[16:17], vcc
	s_cbranch_execz .LBB0_520
	v_add_u32_e32 v1, 48, v77
	v_mad_i64_i32 v[2:3], s[38:39], s19, v1, 0
	v_add_u32_e32 v1, 56, v77
	v_lshl_add_u64 v[2:3], v[2:3], 2, v[78:79]
	v_mad_i64_i32 v[60:61], s[38:39], s19, v1, 0
	v_lshl_add_u64 v[78:79], v[60:61], 2, v[78:79]
	global_load_dwordx4 v[60:63], v[2:3], off nt
	global_load_dwordx4 v[64:67], v[78:79], off nt
